# v35 + MLA/NA KV loops: staging loads in saddr form (no per-load 64-bit VALU add), fmaxf self-max copies folded into their consumers
# baseline (speedup 1.0000x reference)
.LBB0_818:
	s_ashr_i32 s3, s2, 31
	s_mul_hi_u32 s10, s2, s62
	s_mul_i32 s3, s3, s62
	s_add_i32 s3, s10, s3
	s_mul_i32 s2, s2, s62
	s_lshl_b64 s[2:3], s[2:3], 1
	s_add_u32 s10, s8, s2
	s_addc_u32 s11, s9, s3
	s_add_u32 s2, s6, s2
	s_addc_u32 s3, s7, s3
	global_load_dwordx4 v[146:149], v128, s[10:11]
	global_load_dwordx4 v[150:153], v178, s[10:11]
	global_load_dwordx4 v[154:157], v128, s[2:3]
	global_load_dwordx4 v[158:161], v178, s[2:3]
	ds_read_b64_tr_b16 v[212:213], v186 offset:0
	ds_read_b64_tr_b16 v[214:215], v186 offset:0x800
	ds_read_b64_tr_b16 v[216:217], v186 offset:0x1000
	ds_read_b64_tr_b16 v[218:219], v186 offset:0x1800
	ds_read_b64_tr_b16 v[220:221], v186 offset:0x2000
	ds_read_b64_tr_b16 v[222:223], v186 offset:0x2800
	ds_read_b64_tr_b16 v[224:225], v186 offset:0x3000
	ds_read_b64_tr_b16 v[226:227], v186 offset:0x3800
	s_waitcnt lgkmcnt(0)
	s_cmp_lt_u32 s24, 4
	v_mfma_f32_32x32x16_bf16 v[48:63], v[212:215], v[162:165], v[48:63]
	ds_read_b64_tr_b16 v[212:213], v186 offset:0x200
	ds_read_b64_tr_b16 v[214:215], v186 offset:0xa00
	v_mfma_f32_32x32x16_bf16 v[48:63], v[216:219], v[166:169], v[48:63]
	ds_read_b64_tr_b16 v[216:217], v186 offset:0x1200
	ds_read_b64_tr_b16 v[218:219], v186 offset:0x1a00
	v_mfma_f32_32x32x16_bf16 v[48:63], v[220:223], v[170:173], v[48:63]
	ds_read_b64_tr_b16 v[220:221], v186 offset:0x2200
	ds_read_b64_tr_b16 v[222:223], v186 offset:0x2a00
	v_mfma_f32_32x32x16_bf16 v[48:63], v[224:227], v[174:177], v[48:63]
	ds_read_b64_tr_b16 v[224:225], v186 offset:0x3200
	ds_read_b64_tr_b16 v[226:227], v186 offset:0x3a00
	s_waitcnt lgkmcnt(0)
	v_mfma_f32_32x32x16_bf16 v[32:47], v[212:215], v[162:165], v[32:47]
	ds_read_b64_tr_b16 v[212:213], v186 offset:0x400
	ds_read_b64_tr_b16 v[214:215], v186 offset:0xc00
	v_mfma_f32_32x32x16_bf16 v[32:47], v[216:219], v[166:169], v[32:47]
	ds_read_b64_tr_b16 v[216:217], v186 offset:0x1400
	ds_read_b64_tr_b16 v[218:219], v186 offset:0x1c00
	v_mfma_f32_32x32x16_bf16 v[32:47], v[220:223], v[170:173], v[32:47]
	ds_read_b64_tr_b16 v[220:221], v186 offset:0x2400
	ds_read_b64_tr_b16 v[222:223], v186 offset:0x2c00
	v_mfma_f32_32x32x16_bf16 v[32:47], v[224:227], v[174:177], v[32:47]
	ds_read_b64_tr_b16 v[224:225], v186 offset:0x3400
	ds_read_b64_tr_b16 v[226:227], v186 offset:0x3c00
	s_waitcnt lgkmcnt(0)
	v_mfma_f32_32x32x16_bf16 v[16:31], v[212:215], v[162:165], v[16:31]
	ds_read_b64_tr_b16 v[212:213], v186 offset:0x600
	ds_read_b64_tr_b16 v[214:215], v186 offset:0xe00
	v_mfma_f32_32x32x16_bf16 v[16:31], v[216:219], v[166:169], v[16:31]
	ds_read_b64_tr_b16 v[216:217], v186 offset:0x1600
	ds_read_b64_tr_b16 v[218:219], v186 offset:0x1e00
	v_mfma_f32_32x32x16_bf16 v[16:31], v[220:223], v[170:173], v[16:31]
	ds_read_b64_tr_b16 v[220:221], v186 offset:0x2600
	ds_read_b64_tr_b16 v[222:223], v186 offset:0x2e00
	v_mfma_f32_32x32x16_bf16 v[16:31], v[224:227], v[174:177], v[16:31]
	ds_read_b64_tr_b16 v[224:225], v186 offset:0x3600
	ds_read_b64_tr_b16 v[226:227], v186 offset:0x3e00
	s_waitcnt lgkmcnt(0)
	v_mfma_f32_32x32x16_bf16 v[0:15], v[212:215], v[162:165], v[0:15]
	v_mfma_f32_32x32x16_bf16 v[0:15], v[216:219], v[166:169], v[0:15]
	v_mfma_f32_32x32x16_bf16 v[0:15], v[220:223], v[170:173], v[0:15]
	v_mfma_f32_32x32x16_bf16 v[0:15], v[224:227], v[174:177], v[0:15]
	s_cbranch_scc1 .LBB0_822
	s_add_i32 s2, s25, -7
	v_min_i32_e32 v162, s18, v188
	v_cmp_ge_i32_e32 vcc, s2, v185
	v_cmp_le_i32_e64 s[58:59], s2, v162
	s_and_b64 s[2:3], s[58:59], vcc
	v_mov_b32_e32 v177, 0xf149f2ca
	v_mov_b32_e32 v176, 0xf149f2ca
	v_mov_b32_e32 v175, 0xf149f2ca
	v_mov_b32_e32 v174, 0xf149f2ca
	v_mov_b32_e32 v173, 0xf149f2ca
	v_mov_b32_e32 v172, 0xf149f2ca
	v_mov_b32_e32 v171, 0xf149f2ca
	v_mov_b32_e32 v170, 0xf149f2ca
	v_mov_b32_e32 v169, 0xf149f2ca
	v_mov_b32_e32 v168, 0xf149f2ca
	v_mov_b32_e32 v167, 0xf149f2ca
	v_mov_b32_e32 v166, 0xf149f2ca
	v_mov_b32_e32 v165, 0xf149f2ca
	v_mov_b32_e32 v164, 0xf149f2ca
	v_mov_b32_e32 v163, 0xf149f2ca
	v_mov_b32_e32 v162, 0xf149f2ca
	v_mov_b32_e32 v225, 0xf149f2ca
	v_mov_b32_e32 v222, 0xf149f2ca
	v_mov_b32_e32 v221, 0xf149f2ca
	v_mov_b32_e32 v220, 0xf149f2ca
	v_mov_b32_e32 v219, 0xf149f2ca
	v_mov_b32_e32 v218, 0xf149f2ca
	v_mov_b32_e32 v217, 0xf149f2ca
	v_mov_b32_e32 v224, 0xf149f2ca
	v_mov_b32_e32 v223, 0xf149f2ca
	v_mov_b32_e32 v216, 0xf149f2ca
	v_mov_b32_e32 v215, 0xf149f2ca
	v_mov_b32_e32 v214, 0xf149f2ca
	v_mov_b32_e32 v213, 0xf149f2ca
	v_mov_b32_e32 v212, 0xf149f2ca
	v_mov_b32_e32 v211, 0xf149f2ca
	v_mov_b32_e32 v180, 0xf149f2ca
	s_and_saveexec_b64 s[10:11], s[2:3]
	s_cbranch_execz .LBB0_821
	v_mov_b32_e32 v162, v183
	v_mov_b32_e32 v163, v182
	s_movk_i32 s2, 0xffd0
	v_lshlrev_b32_e32 v164, 2, v163
	v_max_i32_e32 v165, 8, v162
	v_lshlrev_b32_e32 v163, 4, v163
	v_lshlrev_b32_e32 v162, 2, v162
	v_sub_u32_e32 v162, v163, v162
	v_add_u32_e32 v194, v208, v162
	ds_read2_b32 v[162:163], v194 offset1:1
	v_add_u32_e32 v165, -8, v165
	v_min_u32_e32 v165, 48, v165
	v_sub_u32_e32 v195, v164, v165
	ds_read2_b32 v[164:165], v194 offset0:2 offset1:3
	ds_read2_b32 v[166:167], v194 offset0:8 offset1:9
	ds_read2_b32 v[168:169], v194 offset0:10 offset1:11
	v_add_u32_e32 v170, 1, v195
	s_waitcnt lgkmcnt(3)
	v_pk_add_f32 v[80:81], v[80:81], v[162:163]
	v_cmp_gt_u32_e32 vcc, 16, v195
	v_add_u32_e32 v171, 3, v195
	v_and_b32_e32 v196, -16, v195
	v_cndmask_b32_e32 v162, v230, v80, vcc
	v_cmp_gt_u32_e32 vcc, 16, v170
	v_add_u32_e32 v170, 2, v195
	v_add_u32_e32 v197, 34, v195
	v_cndmask_b32_e32 v163, v230, v81, vcc
	s_waitcnt lgkmcnt(2)
	v_pk_add_f32 v[80:81], v[82:83], v[164:165]
	v_cmp_gt_u32_e32 vcc, 16, v170
	v_add_u32_e32 v82, 8, v195
	v_add_u32_e32 v83, 9, v195
	v_cndmask_b32_e32 v164, v230, v80, vcc
	v_cmp_gt_u32_e32 vcc, 16, v171
	v_add_u32_e32 v171, 17, v195
	s_nop 0
	v_cndmask_b32_e32 v165, v230, v81, vcc
	s_waitcnt lgkmcnt(1)
	v_pk_add_f32 v[80:81], v[84:85], v[166:167]
	v_cmp_gt_u32_e32 vcc, 16, v82
	v_add_u32_e32 v82, 10, v195
	s_nop 0
	v_cndmask_b32_e32 v166, v230, v80, vcc
	v_cmp_gt_u32_e32 vcc, 16, v83
	v_add_u32_e32 v83, 11, v195
	s_nop 0
	v_cndmask_b32_e32 v167, v230, v81, vcc
	s_waitcnt lgkmcnt(0)
	v_pk_add_f32 v[80:81], v[86:87], v[168:169]
	v_cmp_gt_u32_e32 vcc, 16, v82
	s_nop 1
	v_cndmask_b32_e32 v168, v230, v80, vcc
	v_cmp_gt_u32_e32 vcc, 16, v83
	s_nop 1
	v_cndmask_b32_e32 v169, v230, v81, vcc
	ds_read2_b32 v[80:81], v194 offset0:16 offset1:17
	ds_read2_b32 v[82:83], v194 offset0:18 offset1:19
	ds_read2_b32 v[84:85], v194 offset0:24 offset1:25
	ds_read2_b32 v[86:87], v194 offset0:26 offset1:27
	v_cmp_lt_u32_e32 vcc, s33, v195
	s_waitcnt lgkmcnt(3)
	v_pk_add_f32 v[80:81], v[88:89], v[80:81]
	s_nop 0
	v_cndmask_b32_e32 v170, v230, v80, vcc
	v_cmp_gt_u32_e32 vcc, 16, v171
	v_add_u32_e32 v88, 18, v195
	v_add_u32_e32 v89, 19, v195
	v_cndmask_b32_e32 v171, v230, v81, vcc
	s_waitcnt lgkmcnt(2)
	v_pk_add_f32 v[80:81], v[90:91], v[82:83]
	v_cmp_gt_u32_e32 vcc, 16, v88
	v_add_u32_e32 v82, 24, v195
	v_add_u32_e32 v83, 25, v195
	v_cndmask_b32_e32 v172, v230, v80, vcc
	v_cmp_gt_u32_e32 vcc, 16, v89
	s_nop 1
	v_cndmask_b32_e32 v173, v230, v81, vcc
	s_waitcnt lgkmcnt(1)
	v_pk_add_f32 v[80:81], v[92:93], v[84:85]
	v_cmp_gt_u32_e32 vcc, 16, v82
	v_add_u32_e32 v82, 26, v195
	s_nop 0
	v_cndmask_b32_e32 v174, v230, v80, vcc
	v_cmp_gt_u32_e32 vcc, 16, v83
	v_add_u32_e32 v83, 27, v195
	s_nop 0
	v_cndmask_b32_e32 v175, v230, v81, vcc
	s_waitcnt lgkmcnt(0)
	v_pk_add_f32 v[80:81], v[94:95], v[86:87]
	v_cmp_gt_u32_e32 vcc, 16, v82
	s_nop 1
	v_cndmask_b32_e32 v176, v230, v80, vcc
	v_cmp_gt_u32_e32 vcc, 16, v83
	s_nop 1
	v_cndmask_b32_e32 v177, v230, v81, vcc
	ds_read2_b32 v[80:81], v194 offset0:32 offset1:35
	ds_read2_b32 v[82:83], v194 offset0:40 offset1:43
	ds_read2_b32 v[84:85], v194 offset0:48 offset1:51
	ds_read2_b32 v[86:87], v194 offset0:56 offset1:59
	ds_read2_b32 v[88:89], v194 offset0:33 offset1:34
	s_waitcnt lgkmcnt(4)
	v_add_f32_e32 v64, v64, v80
	v_cmp_eq_u32_e32 vcc, s84, v196
	v_add_u32_e32 v80, 33, v195
	ds_read2_b32 v[90:91], v194 offset0:41 offset1:42
	ds_read2_b32 v[92:93], v194 offset0:49 offset1:50
	ds_read2_b32 v[94:95], v194 offset0:57 offset1:58
	v_cndmask_b32_e32 v180, v230, v64, vcc
	v_mov_b32_e32 v64, v65
	v_mov_b32_e32 v65, v66
	s_waitcnt lgkmcnt(3)
	v_pk_add_f32 v[64:65], v[64:65], v[88:89]
	v_cmp_gt_u32_e32 vcc, 16, v80
	v_add_u32_e32 v80, 35, v195
	v_mov_b32_e32 v66, v81
	v_cndmask_b32_e32 v211, v230, v64, vcc
	v_cmp_gt_u32_e32 vcc, 16, v197
	v_mov_b32_e32 v64, v67
	v_mov_b32_e32 v67, v82
	v_cndmask_b32_e32 v212, v230, v65, vcc
	v_mov_b32_e32 v65, v68
	v_add_u32_e32 v88, 40, v195
	v_pk_add_f32 v[64:65], v[64:65], v[66:67]
	v_cmp_gt_u32_e32 vcc, 16, v80
	v_add_u32_e32 v66, 41, v195
	v_add_u32_e32 v67, 42, v195
	v_cndmask_b32_e32 v213, v230, v64, vcc
	v_cmp_gt_u32_e32 vcc, 16, v88
	v_mov_b32_e32 v64, v69
	v_add_u32_e32 v68, 51, v195
	v_cndmask_b32_e32 v214, v230, v65, vcc
	v_mov_b32_e32 v65, v70
	s_waitcnt lgkmcnt(2)
	v_pk_add_f32 v[64:65], v[64:65], v[90:91]
	v_cmp_gt_u32_e32 vcc, 16, v66
	v_add_u32_e32 v66, 49, v195
	v_add_u32_e32 v69, 56, v195
	v_cndmask_b32_e32 v215, v230, v64, vcc
	v_cmp_gt_u32_e32 vcc, 16, v67
	v_add_u32_e32 v64, 43, v195
	v_add_u32_e32 v67, 50, v195
	v_cndmask_b32_e32 v216, v230, v65, vcc
	v_add_f32_e32 v65, v71, v83
	v_cmp_gt_u32_e32 vcc, 16, v64
	v_add_f32_e32 v64, v72, v84
	s_nop 0
	v_cndmask_b32_e32 v223, v230, v65, vcc
	v_cmp_eq_u32_e32 vcc, s2, v196
	v_mov_b32_e32 v65, v74
	s_nop 0
	v_cndmask_b32_e32 v224, v230, v64, vcc
	v_mov_b32_e32 v64, v73
	s_waitcnt lgkmcnt(1)
	v_pk_add_f32 v[64:65], v[64:65], v[92:93]
	v_cmp_gt_u32_e32 vcc, 16, v66
	v_mov_b32_e32 v66, v85
	s_nop 0
	v_cndmask_b32_e32 v217, v230, v64, vcc
	v_cmp_gt_u32_e32 vcc, 16, v67
	v_mov_b32_e32 v64, v75
	v_mov_b32_e32 v67, v86
	v_cndmask_b32_e32 v218, v230, v65, vcc
	v_mov_b32_e32 v65, v76
	v_pk_add_f32 v[64:65], v[64:65], v[66:67]
	v_cmp_gt_u32_e32 vcc, 16, v68
	v_add_u32_e32 v66, 57, v195
	v_add_u32_e32 v67, 58, v195
	v_cndmask_b32_e32 v219, v230, v64, vcc
	v_cmp_gt_u32_e32 vcc, 16, v69
	v_mov_b32_e32 v64, v77
	s_nop 0
	v_cndmask_b32_e32 v220, v230, v65, vcc
	v_mov_b32_e32 v65, v78
	s_waitcnt lgkmcnt(0)
	v_pk_add_f32 v[64:65], v[64:65], v[94:95]
	v_cmp_gt_u32_e32 vcc, 16, v66
	s_nop 1
	v_cndmask_b32_e32 v221, v230, v64, vcc
	v_cmp_gt_u32_e32 vcc, 16, v67
	v_add_u32_e32 v64, 59, v195
	s_nop 0
	v_cndmask_b32_e32 v222, v230, v65, vcc
	v_add_f32_e32 v65, v79, v87
	v_cmp_gt_u32_e32 vcc, 16, v64
	s_nop 1
	v_cndmask_b32_e32 v225, v230, v65, vcc

.LBB0_823:
	v_max_f32_e32 v65, v162, v163
	v_max_f32_e32 v66, v170, v171
	v_max_f32_e32 v67, v72, v217
	v_max3_f32 v68, v64, v211, v212
	v_max3_f32 v67, v67, v218, v219
	v_max3_f32 v65, v65, v164, v165
	v_max3_f32 v66, v66, v172, v173
	v_max3_f32 v68, v68, v213, v214
	v_max3_f32 v67, v67, v220, v221
	v_max3_f32 v65, v65, v166, v167
	v_max3_f32 v66, v66, v174, v175
	v_max3_f32 v68, v68, v215, v216
	v_max3_f32 v67, v67, v222, v79
	v_max3_f32 v65, v65, v168, v169
	v_max3_f32 v66, v66, v176, v177
	v_max3_f32 v67, v68, v71, v67
	v_max3_f32 v65, v65, v66, v67
	v_mov_b32_e32 v66, v65
	s_nop 1
	v_permlane32_swap_b32_e32 v65, v66
	v_max_f32_e32 v65, v65, v66
	v_sub_f32_e32 v66, v65, v206
	v_max_f32_e32 v65, v206, v65
	v_sub_f32_e32 v67, v206, v65
	v_mul_f32_e32 v67, 0x3e0293ee, v67
	v_exp_f32_e32 v67, v67
	v_cmp_ge_f32_e32 vcc, s31, v66
	s_cmp_eq_u64 vcc, exec
	s_cselect_b64 s[58:59], -1, 0
	s_barrier
	s_waitcnt vmcnt(4)
	v_cndmask_b32_e64 v180, v67, 1.0, s[58:59]
	v_cmp_gt_f32_e32 vcc, 1.0, v180
	s_waitcnt vmcnt(7)
	ds_write_b128 v201, v[130:133]
	s_waitcnt vmcnt(6)
	ds_write_b128 v202, v[134:137]
	s_waitcnt vmcnt(5)
	ds_write_b128 v203, v[138:141] offset:32768
	s_waitcnt vmcnt(4)
	ds_write_b128 v204, v[142:145] offset:32768
	s_cbranch_vccz .LBB0_825
	v_pk_mul_f32 v[62:63], v[62:63], v[180:181] op_sel_hi:[1,0]
	v_pk_mul_f32 v[60:61], v[60:61], v[180:181] op_sel_hi:[1,0]
	v_pk_mul_f32 v[58:59], v[58:59], v[180:181] op_sel_hi:[1,0]
	v_pk_mul_f32 v[56:57], v[56:57], v[180:181] op_sel_hi:[1,0]
	v_pk_mul_f32 v[54:55], v[54:55], v[180:181] op_sel_hi:[1,0]
	v_pk_mul_f32 v[52:53], v[52:53], v[180:181] op_sel_hi:[1,0]
	v_pk_mul_f32 v[50:51], v[50:51], v[180:181] op_sel_hi:[1,0]
	v_pk_mul_f32 v[48:49], v[48:49], v[180:181] op_sel_hi:[1,0]
	v_pk_mul_f32 v[46:47], v[46:47], v[180:181] op_sel_hi:[1,0]
	v_pk_mul_f32 v[44:45], v[44:45], v[180:181] op_sel_hi:[1,0]
	v_pk_mul_f32 v[42:43], v[42:43], v[180:181] op_sel_hi:[1,0]
	v_pk_mul_f32 v[40:41], v[40:41], v[180:181] op_sel_hi:[1,0]
	v_pk_mul_f32 v[38:39], v[38:39], v[180:181] op_sel_hi:[1,0]
	v_pk_mul_f32 v[36:37], v[36:37], v[180:181] op_sel_hi:[1,0]
	v_pk_mul_f32 v[34:35], v[34:35], v[180:181] op_sel_hi:[1,0]
	v_pk_mul_f32 v[32:33], v[32:33], v[180:181] op_sel_hi:[1,0]
	v_pk_mul_f32 v[30:31], v[30:31], v[180:181] op_sel_hi:[1,0]
	v_pk_mul_f32 v[28:29], v[28:29], v[180:181] op_sel_hi:[1,0]
	v_pk_mul_f32 v[26:27], v[26:27], v[180:181] op_sel_hi:[1,0]
	v_pk_mul_f32 v[24:25], v[24:25], v[180:181] op_sel_hi:[1,0]
	v_pk_mul_f32 v[22:23], v[22:23], v[180:181] op_sel_hi:[1,0]
	v_pk_mul_f32 v[20:21], v[20:21], v[180:181] op_sel_hi:[1,0]
	v_pk_mul_f32 v[18:19], v[18:19], v[180:181] op_sel_hi:[1,0]
	v_pk_mul_f32 v[16:17], v[16:17], v[180:181] op_sel_hi:[1,0]
	v_pk_mul_f32 v[14:15], v[14:15], v[180:181] op_sel_hi:[1,0]
	v_pk_mul_f32 v[12:13], v[12:13], v[180:181] op_sel_hi:[1,0]
	v_pk_mul_f32 v[10:11], v[10:11], v[180:181] op_sel_hi:[1,0]
	v_pk_mul_f32 v[8:9], v[8:9], v[180:181] op_sel_hi:[1,0]
	v_pk_mul_f32 v[6:7], v[6:7], v[180:181] op_sel_hi:[1,0]
	v_pk_mul_f32 v[4:5], v[4:5], v[180:181] op_sel_hi:[1,0]
	v_pk_mul_f32 v[2:3], v[2:3], v[180:181] op_sel_hi:[1,0]
	v_pk_mul_f32 v[0:1], v[0:1], v[180:181] op_sel_hi:[1,0]

.LBB0_829:
	s_ashr_i32 s3, s2, 31
	s_mul_hi_u32 s10, s2, s62
	s_mul_i32 s3, s3, s62
	s_add_i32 s3, s10, s3
	s_mul_i32 s2, s2, s62
	s_lshl_b64 s[2:3], s[2:3], 1
	s_add_u32 s10, s8, s2
	s_addc_u32 s11, s9, s3
	s_add_u32 s2, s6, s2
	s_addc_u32 s3, s7, s3
	global_load_dwordx4 v[130:133], v128, s[10:11]
	global_load_dwordx4 v[134:137], v178, s[10:11]
	global_load_dwordx4 v[138:141], v128, s[2:3]
	global_load_dwordx4 v[142:145], v178, s[2:3]
	ds_read_b64_tr_b16 v[214:215], v207 offset:0
	ds_read_b64_tr_b16 v[216:217], v207 offset:0x800
	ds_read_b64_tr_b16 v[218:219], v207 offset:0x1000
	ds_read_b64_tr_b16 v[220:221], v207 offset:0x1800
	ds_read_b64_tr_b16 v[222:223], v207 offset:0x2000
	ds_read_b64_tr_b16 v[224:225], v207 offset:0x2800
	ds_read_b64_tr_b16 v[226:227], v207 offset:0x3000
	ds_read_b64_tr_b16 v[228:229], v207 offset:0x3800
	s_waitcnt lgkmcnt(0)
	s_cmp_lt_u32 s24, 3
	v_mfma_f32_32x32x16_bf16 v[48:63], v[214:217], v[162:165], v[48:63]
	ds_read_b64_tr_b16 v[214:215], v207 offset:0x200
	ds_read_b64_tr_b16 v[216:217], v207 offset:0xa00
	v_mfma_f32_32x32x16_bf16 v[48:63], v[218:221], v[166:169], v[48:63]
	ds_read_b64_tr_b16 v[218:219], v207 offset:0x1200
	ds_read_b64_tr_b16 v[220:221], v207 offset:0x1a00
	v_mfma_f32_32x32x16_bf16 v[48:63], v[222:225], v[170:173], v[48:63]
	ds_read_b64_tr_b16 v[222:223], v207 offset:0x2200
	ds_read_b64_tr_b16 v[224:225], v207 offset:0x2a00
	v_mfma_f32_32x32x16_bf16 v[48:63], v[226:229], v[174:177], v[48:63]
	ds_read_b64_tr_b16 v[226:227], v207 offset:0x3200
	ds_read_b64_tr_b16 v[228:229], v207 offset:0x3a00
	s_waitcnt lgkmcnt(0)
	v_mfma_f32_32x32x16_bf16 v[32:47], v[214:217], v[162:165], v[32:47]
	ds_read_b64_tr_b16 v[214:215], v207 offset:0x400
	ds_read_b64_tr_b16 v[216:217], v207 offset:0xc00
	v_mfma_f32_32x32x16_bf16 v[32:47], v[218:221], v[166:169], v[32:47]
	ds_read_b64_tr_b16 v[218:219], v207 offset:0x1400
	ds_read_b64_tr_b16 v[220:221], v207 offset:0x1c00
	v_mfma_f32_32x32x16_bf16 v[32:47], v[222:225], v[170:173], v[32:47]
	ds_read_b64_tr_b16 v[222:223], v207 offset:0x2400
	ds_read_b64_tr_b16 v[224:225], v207 offset:0x2c00
	v_mfma_f32_32x32x16_bf16 v[32:47], v[226:229], v[174:177], v[32:47]
	ds_read_b64_tr_b16 v[226:227], v207 offset:0x3400
	ds_read_b64_tr_b16 v[228:229], v207 offset:0x3c00
	s_waitcnt lgkmcnt(0)
	v_mfma_f32_32x32x16_bf16 v[16:31], v[214:217], v[162:165], v[16:31]
	ds_read_b64_tr_b16 v[214:215], v207 offset:0x600
	ds_read_b64_tr_b16 v[216:217], v207 offset:0xe00
	v_mfma_f32_32x32x16_bf16 v[16:31], v[218:221], v[166:169], v[16:31]
	ds_read_b64_tr_b16 v[218:219], v207 offset:0x1600
	ds_read_b64_tr_b16 v[220:221], v207 offset:0x1e00
	v_mfma_f32_32x32x16_bf16 v[16:31], v[222:225], v[170:173], v[16:31]
	ds_read_b64_tr_b16 v[222:223], v207 offset:0x2600
	ds_read_b64_tr_b16 v[224:225], v207 offset:0x2e00
	v_mfma_f32_32x32x16_bf16 v[16:31], v[226:229], v[174:177], v[16:31]
	ds_read_b64_tr_b16 v[226:227], v207 offset:0x3600
	ds_read_b64_tr_b16 v[228:229], v207 offset:0x3e00
	s_waitcnt lgkmcnt(0)
	v_mfma_f32_32x32x16_bf16 v[0:15], v[214:217], v[162:165], v[0:15]
	v_mfma_f32_32x32x16_bf16 v[0:15], v[218:221], v[166:169], v[0:15]
	v_mfma_f32_32x32x16_bf16 v[0:15], v[222:225], v[170:173], v[0:15]
	v_mfma_f32_32x32x16_bf16 v[0:15], v[226:229], v[174:177], v[0:15]
	s_cbranch_scc1 .LBB0_833
	s_add_i32 s2, s25, -6
	v_min_i32_e32 v162, s18, v188
	v_cmp_ge_i32_e32 vcc, s2, v185
	v_cmp_le_i32_e64 s[58:59], s2, v162
	s_and_b64 s[2:3], s[58:59], vcc
	v_mov_b32_e32 v220, 0xf149f2ca
	v_mov_b32_e32 v221, 0xf149f2ca
	v_mov_b32_e32 v219, 0xf149f2ca
	v_mov_b32_e32 v218, 0xf149f2ca
	v_mov_b32_e32 v217, 0xf149f2ca
	v_mov_b32_e32 v216, 0xf149f2ca
	v_mov_b32_e32 v215, 0xf149f2ca
	v_mov_b32_e32 v214, 0xf149f2ca
	v_mov_b32_e32 v211, 0xf149f2ca
	v_mov_b32_e32 v177, 0xf149f2ca
	v_mov_b32_e32 v176, 0xf149f2ca
	v_mov_b32_e32 v175, 0xf149f2ca
	v_mov_b32_e32 v174, 0xf149f2ca
	v_mov_b32_e32 v173, 0xf149f2ca
	v_mov_b32_e32 v172, 0xf149f2ca
	v_mov_b32_e32 v163, 0xf149f2ca
	v_mov_b32_e32 v228, 0xf149f2ca
	v_mov_b32_e32 v227, 0xf149f2ca
	v_mov_b32_e32 v171, 0xf149f2ca
	v_mov_b32_e32 v170, 0xf149f2ca
	v_mov_b32_e32 v169, 0xf149f2ca
	v_mov_b32_e32 v168, 0xf149f2ca
	v_mov_b32_e32 v226, 0xf149f2ca
	v_mov_b32_e32 v225, 0xf149f2ca
	v_mov_b32_e32 v224, 0xf149f2ca
	v_mov_b32_e32 v223, 0xf149f2ca
	v_mov_b32_e32 v167, 0xf149f2ca
	v_mov_b32_e32 v166, 0xf149f2ca
	v_mov_b32_e32 v165, 0xf149f2ca
	v_mov_b32_e32 v164, 0xf149f2ca
	v_mov_b32_e32 v222, 0xf149f2ca
	v_mov_b32_e32 v162, 0xf149f2ca
	s_and_saveexec_b64 s[10:11], s[2:3]
	s_cbranch_execz .LBB0_832
	v_mov_b32_e32 v162, v183
	v_mov_b32_e32 v163, v182
	s_movk_i32 s2, 0xffd0
	v_lshlrev_b32_e32 v164, 2, v163
	v_max_i32_e32 v165, 8, v162
	v_lshlrev_b32_e32 v163, 4, v163
	v_lshlrev_b32_e32 v162, 2, v162
	v_sub_u32_e32 v162, v163, v162
	v_add_u32_e32 v170, v208, v162
	ds_read2_b32 v[162:163], v170 offset0:31 offset1:32
	v_add_u32_e32 v165, -8, v165
	v_min_u32_e32 v165, 48, v165
	v_sub_u32_e32 v194, v164, v165
	ds_read2_b32 v[164:165], v170 offset0:33 offset1:34
	ds_read2_b32 v[166:167], v170 offset0:39 offset1:40
	ds_read2_b32 v[168:169], v170 offset0:41 offset1:42
	v_add_u32_e32 v171, 1, v194
	s_waitcnt lgkmcnt(3)
	v_pk_add_f32 v[80:81], v[80:81], v[162:163]
	v_cmp_gt_u32_e32 vcc, 16, v194
	v_add_u32_e32 v162, 2, v194
	s_nop 0
	v_cndmask_b32_e32 v163, v230, v80, vcc
	v_cmp_gt_u32_e32 vcc, 16, v171
	v_add_u32_e32 v171, 3, v194
	s_nop 0
	v_cndmask_b32_e32 v172, v230, v81, vcc
	s_waitcnt lgkmcnt(2)
	v_pk_add_f32 v[80:81], v[82:83], v[164:165]
	v_cmp_gt_u32_e32 vcc, 16, v162
	v_add_u32_e32 v82, 8, v194
	v_add_u32_e32 v83, 9, v194
	v_cndmask_b32_e32 v173, v230, v80, vcc
	v_cmp_gt_u32_e32 vcc, 16, v171
	v_add_u32_e32 v162, 17, v194
	v_add_u32_e32 v164, 34, v194
	v_cndmask_b32_e32 v174, v230, v81, vcc
	s_waitcnt lgkmcnt(1)
	v_pk_add_f32 v[80:81], v[84:85], v[166:167]
	v_cmp_gt_u32_e32 vcc, 16, v82
	v_add_u32_e32 v82, 10, v194
	s_nop 0
	v_cndmask_b32_e32 v175, v230, v80, vcc
	v_cmp_gt_u32_e32 vcc, 16, v83
	v_add_u32_e32 v83, 11, v194
	s_nop 0
	v_cndmask_b32_e32 v176, v230, v81, vcc
	s_waitcnt lgkmcnt(0)
	v_pk_add_f32 v[80:81], v[86:87], v[168:169]
	v_cmp_gt_u32_e32 vcc, 16, v82
	v_and_b32_e32 v168, -16, v194
	s_nop 0
	v_cndmask_b32_e32 v177, v230, v80, vcc
	v_cmp_gt_u32_e32 vcc, 16, v83
	s_nop 1
	v_cndmask_b32_e32 v211, v230, v81, vcc
	ds_read2_b32 v[80:81], v170 offset0:47 offset1:48
	ds_read2_b32 v[82:83], v170 offset0:49 offset1:50
	ds_read2_b32 v[84:85], v170 offset0:55 offset1:56
	ds_read2_b32 v[86:87], v170 offset0:57 offset1:58
	v_cmp_lt_u32_e32 vcc, s33, v194
	s_waitcnt lgkmcnt(3)
	v_pk_add_f32 v[80:81], v[88:89], v[80:81]
	s_nop 0
	v_cndmask_b32_e32 v214, v230, v80, vcc
	v_cmp_gt_u32_e32 vcc, 16, v162
	v_add_u32_e32 v88, 18, v194
	v_add_u32_e32 v89, 19, v194
	v_cndmask_b32_e32 v215, v230, v81, vcc
	s_waitcnt lgkmcnt(2)
	v_pk_add_f32 v[80:81], v[90:91], v[82:83]
	v_cmp_gt_u32_e32 vcc, 16, v88
	v_add_u32_e32 v82, 24, v194
	v_add_u32_e32 v83, 25, v194
	v_cndmask_b32_e32 v216, v230, v80, vcc
	v_cmp_gt_u32_e32 vcc, 16, v89
	s_nop 1
	v_cndmask_b32_e32 v217, v230, v81, vcc
	s_waitcnt lgkmcnt(1)
	v_pk_add_f32 v[80:81], v[92:93], v[84:85]
	v_cmp_gt_u32_e32 vcc, 16, v82
	v_add_u32_e32 v82, 26, v194
	s_nop 0
	v_cndmask_b32_e32 v218, v230, v80, vcc
	v_cmp_gt_u32_e32 vcc, 16, v83
	v_add_u32_e32 v83, 27, v194
	s_nop 0
	v_cndmask_b32_e32 v219, v230, v81, vcc
	s_waitcnt lgkmcnt(0)
	v_pk_add_f32 v[80:81], v[94:95], v[86:87]
	v_cmp_gt_u32_e32 vcc, 16, v82
	s_nop 1
	v_cndmask_b32_e32 v221, v230, v80, vcc
	v_cmp_gt_u32_e32 vcc, 16, v83
	s_nop 1
	v_cndmask_b32_e32 v220, v230, v81, vcc
	ds_read2_b32 v[80:81], v170 offset0:63 offset1:66
	ds_read2_b32 v[82:83], v170 offset0:71 offset1:74
	ds_read2_b32 v[84:85], v170 offset0:79 offset1:82
	ds_read2_b32 v[86:87], v170 offset0:87 offset1:90
	ds_read2_b32 v[88:89], v170 offset0:64 offset1:65
	s_waitcnt lgkmcnt(4)
	v_add_f32_e32 v64, v64, v80
	v_cmp_eq_u32_e32 vcc, s84, v168
	v_add_u32_e32 v80, 33, v194
	ds_read2_b32 v[90:91], v170 offset0:72 offset1:73
	ds_read2_b32 v[92:93], v170 offset0:80 offset1:81
	ds_read2_b32 v[94:95], v170 offset0:88 offset1:89
	v_cndmask_b32_e32 v162, v230, v64, vcc
	v_mov_b32_e32 v64, v65
	v_mov_b32_e32 v65, v66
	s_waitcnt lgkmcnt(3)
	v_pk_add_f32 v[64:65], v[64:65], v[88:89]
	v_cmp_gt_u32_e32 vcc, 16, v80
	v_add_u32_e32 v80, 35, v194
	v_mov_b32_e32 v66, v81
	v_cndmask_b32_e32 v222, v230, v64, vcc
	v_cmp_gt_u32_e32 vcc, 16, v164
	v_mov_b32_e32 v64, v67
	v_mov_b32_e32 v67, v82
	v_cndmask_b32_e32 v164, v230, v65, vcc
	v_mov_b32_e32 v65, v68
	v_add_u32_e32 v88, 40, v194
	v_pk_add_f32 v[64:65], v[64:65], v[66:67]
	v_cmp_gt_u32_e32 vcc, 16, v80
	v_add_u32_e32 v66, 41, v194
	v_add_u32_e32 v67, 42, v194
	v_cndmask_b32_e32 v165, v230, v64, vcc
	v_cmp_gt_u32_e32 vcc, 16, v88
	v_mov_b32_e32 v64, v69
	v_add_u32_e32 v68, 51, v194
	v_cndmask_b32_e32 v166, v230, v65, vcc
	v_mov_b32_e32 v65, v70
	s_waitcnt lgkmcnt(2)
	v_pk_add_f32 v[64:65], v[64:65], v[90:91]
	v_cmp_gt_u32_e32 vcc, 16, v66
	v_add_u32_e32 v66, 49, v194
	v_add_u32_e32 v69, 56, v194
	v_cndmask_b32_e32 v167, v230, v64, vcc
	v_cmp_gt_u32_e32 vcc, 16, v67
	v_add_u32_e32 v64, 43, v194
	v_add_u32_e32 v67, 50, v194
	v_cndmask_b32_e32 v223, v230, v65, vcc
	v_add_f32_e32 v65, v71, v83
	v_cmp_gt_u32_e32 vcc, 16, v64
	v_add_f32_e32 v64, v72, v84
	s_nop 0
	v_cndmask_b32_e32 v224, v230, v65, vcc
	v_cmp_eq_u32_e32 vcc, s2, v168
	v_mov_b32_e32 v65, v74
	s_nop 0
	v_cndmask_b32_e32 v225, v230, v64, vcc
	v_mov_b32_e32 v64, v73
	s_waitcnt lgkmcnt(1)
	v_pk_add_f32 v[64:65], v[64:65], v[92:93]
	v_cmp_gt_u32_e32 vcc, 16, v66
	v_mov_b32_e32 v66, v85
	s_nop 0
	v_cndmask_b32_e32 v226, v230, v64, vcc
	v_cmp_gt_u32_e32 vcc, 16, v67
	v_mov_b32_e32 v64, v75
	v_mov_b32_e32 v67, v86
	v_cndmask_b32_e32 v168, v230, v65, vcc
	v_mov_b32_e32 v65, v76
	v_pk_add_f32 v[64:65], v[64:65], v[66:67]
	v_cmp_gt_u32_e32 vcc, 16, v68
	v_add_u32_e32 v66, 57, v194
	v_add_u32_e32 v67, 58, v194
	v_cndmask_b32_e32 v169, v230, v64, vcc
	v_cmp_gt_u32_e32 vcc, 16, v69
	v_mov_b32_e32 v64, v77
	s_nop 0
	v_cndmask_b32_e32 v170, v230, v65, vcc
	v_mov_b32_e32 v65, v78
	s_waitcnt lgkmcnt(0)
	v_pk_add_f32 v[64:65], v[64:65], v[94:95]
	v_cmp_gt_u32_e32 vcc, 16, v66
	s_nop 1
	v_cndmask_b32_e32 v171, v230, v64, vcc
	v_cmp_gt_u32_e32 vcc, 16, v67
	v_add_u32_e32 v64, 59, v194
	s_nop 0
	v_cndmask_b32_e32 v227, v230, v65, vcc
	v_add_f32_e32 v65, v79, v87
	v_cmp_gt_u32_e32 vcc, 16, v64
	s_nop 1
	v_cndmask_b32_e32 v228, v230, v65, vcc

.LBB0_834:
	v_max_f32_e32 v66, v163, v172
	v_max_f32_e32 v67, v214, v215
	v_max_f32_e32 v68, v72, v73
	v_max3_f32 v69, v64, v65, v164
	v_max3_f32 v68, v68, v168, v169
	v_max3_f32 v66, v66, v173, v174
	v_max3_f32 v67, v67, v216, v217
	v_max3_f32 v69, v69, v165, v166
	v_max3_f32 v68, v68, v170, v171
	v_max3_f32 v66, v66, v175, v176
	v_max3_f32 v67, v67, v218, v219
	v_max3_f32 v69, v69, v167, v70
	v_max3_f32 v68, v68, v78, v79
	v_max3_f32 v66, v66, v177, v211
	v_max3_f32 v67, v67, v221, v220
	v_max3_f32 v68, v69, v71, v68
	v_max3_f32 v66, v66, v67, v68
	v_mov_b32_e32 v67, v66
	s_nop 1
	v_permlane32_swap_b32_e32 v66, v67
	v_max_f32_e32 v66, v66, v67
	v_sub_f32_e32 v67, v66, v206
	v_max_f32_e32 v66, v206, v66
	v_sub_f32_e32 v68, v206, v66
	v_mul_f32_e32 v68, 0x3e0293ee, v68
	v_exp_f32_e32 v68, v68
	v_cmp_ge_f32_e32 vcc, s31, v67
	s_cmp_eq_u64 vcc, exec
	s_cselect_b64 s[58:59], -1, 0
	s_barrier
	s_waitcnt vmcnt(4)
	v_cndmask_b32_e64 v162, v68, 1.0, s[58:59]
	v_cmp_gt_f32_e32 vcc, 1.0, v162
	s_waitcnt vmcnt(7)
	ds_write_b128 v201, v[146:149] offset:16384
	s_waitcnt vmcnt(6)
	ds_write_b128 v202, v[150:153] offset:16384
	s_waitcnt vmcnt(5)
	ds_write_b128 v203, v[154:157] offset:49152
	s_waitcnt vmcnt(4)
	ds_write_b128 v204, v[158:161] offset:49152
	s_cbranch_vccz .LBB0_836
	v_pk_mul_f32 v[62:63], v[62:63], v[162:163] op_sel_hi:[1,0]
	v_pk_mul_f32 v[60:61], v[60:61], v[162:163] op_sel_hi:[1,0]
	v_pk_mul_f32 v[58:59], v[58:59], v[162:163] op_sel_hi:[1,0]
	v_pk_mul_f32 v[56:57], v[56:57], v[162:163] op_sel_hi:[1,0]
	v_pk_mul_f32 v[54:55], v[54:55], v[162:163] op_sel_hi:[1,0]
	v_pk_mul_f32 v[52:53], v[52:53], v[162:163] op_sel_hi:[1,0]
	v_pk_mul_f32 v[50:51], v[50:51], v[162:163] op_sel_hi:[1,0]
	v_pk_mul_f32 v[48:49], v[48:49], v[162:163] op_sel_hi:[1,0]
	v_pk_mul_f32 v[46:47], v[46:47], v[162:163] op_sel_hi:[1,0]
	v_pk_mul_f32 v[44:45], v[44:45], v[162:163] op_sel_hi:[1,0]
	v_pk_mul_f32 v[42:43], v[42:43], v[162:163] op_sel_hi:[1,0]
	v_pk_mul_f32 v[40:41], v[40:41], v[162:163] op_sel_hi:[1,0]
	v_pk_mul_f32 v[38:39], v[38:39], v[162:163] op_sel_hi:[1,0]
	v_pk_mul_f32 v[36:37], v[36:37], v[162:163] op_sel_hi:[1,0]
	v_pk_mul_f32 v[34:35], v[34:35], v[162:163] op_sel_hi:[1,0]
	v_pk_mul_f32 v[32:33], v[32:33], v[162:163] op_sel_hi:[1,0]
	v_pk_mul_f32 v[30:31], v[30:31], v[162:163] op_sel_hi:[1,0]
	v_pk_mul_f32 v[28:29], v[28:29], v[162:163] op_sel_hi:[1,0]
	v_pk_mul_f32 v[26:27], v[26:27], v[162:163] op_sel_hi:[1,0]
	v_pk_mul_f32 v[24:25], v[24:25], v[162:163] op_sel_hi:[1,0]
	v_pk_mul_f32 v[22:23], v[22:23], v[162:163] op_sel_hi:[1,0]
	v_pk_mul_f32 v[20:21], v[20:21], v[162:163] op_sel_hi:[1,0]
	v_pk_mul_f32 v[18:19], v[18:19], v[162:163] op_sel_hi:[1,0]
	v_pk_mul_f32 v[16:17], v[16:17], v[162:163] op_sel_hi:[1,0]
	v_pk_mul_f32 v[14:15], v[14:15], v[162:163] op_sel_hi:[1,0]
	v_pk_mul_f32 v[12:13], v[12:13], v[162:163] op_sel_hi:[1,0]
	v_pk_mul_f32 v[10:11], v[10:11], v[162:163] op_sel_hi:[1,0]
	v_pk_mul_f32 v[8:9], v[8:9], v[162:163] op_sel_hi:[1,0]
	v_pk_mul_f32 v[6:7], v[6:7], v[162:163] op_sel_hi:[1,0]
	v_pk_mul_f32 v[4:5], v[4:5], v[162:163] op_sel_hi:[1,0]
	v_pk_mul_f32 v[2:3], v[2:3], v[162:163] op_sel_hi:[1,0]
	v_pk_mul_f32 v[0:1], v[0:1], v[162:163] op_sel_hi:[1,0]

.LBB0_861:
	ds_read_b128 v[96:99], v209 offset:49152
	ds_read_b128 v[100:103], v209 offset:57344
	ds_read_b128 v[162:165], v211 offset:49152
	ds_read_b128 v[166:169], v211 offset:57344
	s_add_i32 s2, 0, 0x12000
	v_add_u32_e32 v233, s2, v218
	s_waitcnt lgkmcnt(3)
	v_mfma_f32_32x32x16_bf16 v[112:127], v[96:99], v[158:161], 0
	v_add_u32_e32 v234, s2, v220
	v_add_u32_e32 v236, s2, v222
	v_add_u32_e32 v235, s2, v224
	v_exp_f32_e32 v80, v80
	v_exp_f32_e32 v81, v81
	v_exp_f32_e32 v82, v82
	v_exp_f32_e32 v83, v83
	s_waitcnt lgkmcnt(2)
	v_mfma_f32_32x32x16_bf16 v[96:111], v[100:103], v[158:161], 0
	v_exp_f32_e32 v84, v84
	v_exp_f32_e32 v92, v92
	v_exp_f32_e32 v85, v85
	v_exp_f32_e32 v93, v93
	v_exp_f32_e32 v86, v86
	v_exp_f32_e32 v94, v94
	v_exp_f32_e32 v87, v87
	s_waitcnt lgkmcnt(1)
	v_mfma_f32_32x32x16_bf16 v[112:127], v[162:165], v[154:157], v[112:127]
	v_exp_f32_e32 v95, v95
	s_waitcnt lgkmcnt(0)
	v_mfma_f32_32x32x16_bf16 v[96:111], v[166:169], v[154:157], v[96:111]
	ds_read_b128 v[162:165], v212 offset:49152
	ds_read_b128 v[166:169], v212 offset:57344
	s_waitcnt lgkmcnt(1)
	v_mfma_f32_32x32x16_bf16 v[112:127], v[162:165], v[150:153], v[112:127]
	s_waitcnt lgkmcnt(0)
	v_mfma_f32_32x32x16_bf16 v[96:111], v[166:169], v[150:153], v[96:111]
	ds_read_b128 v[162:165], v213 offset:49152
	ds_read_b128 v[166:169], v213 offset:57344
	s_waitcnt lgkmcnt(1)
	v_mfma_f32_32x32x16_bf16 v[112:127], v[162:165], v[146:149], v[112:127]
	s_waitcnt lgkmcnt(0)
	v_mfma_f32_32x32x16_bf16 v[96:111], v[166:169], v[146:149], v[96:111]
	ds_read_b128 v[162:165], v215 offset:49152
	ds_read_b128 v[166:169], v215 offset:57344
	s_waitcnt lgkmcnt(1)
	v_mfma_f32_32x32x16_bf16 v[112:127], v[162:165], v[142:145], v[112:127]
	s_waitcnt lgkmcnt(0)
	v_mfma_f32_32x32x16_bf16 v[96:111], v[166:169], v[142:145], v[96:111]
	ds_read_b128 v[162:165], v217 offset:49152
	ds_read_b128 v[166:169], v217 offset:57344
	s_waitcnt lgkmcnt(1)
	v_mfma_f32_32x32x16_bf16 v[112:127], v[162:165], v[138:141], v[112:127]
	s_waitcnt lgkmcnt(0)
	v_mfma_f32_32x32x16_bf16 v[96:111], v[166:169], v[138:141], v[96:111]
	ds_read_b128 v[162:165], v214 offset:49152
	ds_read_b128 v[166:169], v214 offset:57344
	s_waitcnt lgkmcnt(1)
	v_mfma_f32_32x32x16_bf16 v[112:127], v[162:165], v[134:137], v[112:127]
	s_waitcnt lgkmcnt(0)
	v_mfma_f32_32x32x16_bf16 v[96:111], v[166:169], v[134:137], v[96:111]
	ds_read_b128 v[162:165], v216 offset:49152
	ds_read_b128 v[166:169], v216 offset:57344
	s_waitcnt lgkmcnt(1)
	v_mfma_f32_32x32x16_bf16 v[112:127], v[162:165], v[130:133], v[112:127]
	s_waitcnt lgkmcnt(0)
	v_mfma_f32_32x32x16_bf16 v[96:111], v[166:169], v[130:133], v[96:111]
	ds_read_b128 v[162:165], v233
	ds_read_b128 v[166:169], v233 offset:4096
	ds_read_b128 v[170:173], v204
	s_waitcnt lgkmcnt(0)
	v_mfma_f32_32x32x16_bf16 v[112:127], v[162:165], v[170:173], v[112:127]
	v_mfma_f32_32x32x16_bf16 v[96:111], v[166:169], v[170:173], v[96:111]
	ds_read_b128 v[162:165], v234
	ds_read_b128 v[166:169], v234 offset:4096
	ds_read_b128 v[170:173], v204 offset:1024
	s_waitcnt lgkmcnt(0)
	v_mfma_f32_32x32x16_bf16 v[112:127], v[162:165], v[170:173], v[112:127]
	v_mfma_f32_32x32x16_bf16 v[96:111], v[166:169], v[170:173], v[96:111]
	ds_read_b128 v[162:165], v236
	ds_read_b128 v[166:169], v236 offset:4096
	ds_read_b128 v[170:173], v204 offset:2048
	s_waitcnt lgkmcnt(0)
	v_mfma_f32_32x32x16_bf16 v[112:127], v[162:165], v[170:173], v[112:127]
	v_mfma_f32_32x32x16_bf16 v[96:111], v[166:169], v[170:173], v[96:111]
	ds_read_b128 v[162:165], v235
	ds_read_b128 v[166:169], v235 offset:4096
	ds_read_b128 v[170:173], v204 offset:3072
	s_waitcnt lgkmcnt(0)
	v_mfma_f32_32x32x16_bf16 v[112:127], v[162:165], v[170:173], v[112:127]
	v_exp_f32_e32 v162, v88
	v_exp_f32_e32 v163, v89
	v_exp_f32_e32 v164, v90
	v_exp_f32_e32 v165, v91
	v_add_f32_e32 v88, v64, v65
	v_add_f32_e32 v89, v72, v73
	v_add_f32_e32 v90, v80, v81
	v_add_f32_e32 v91, v162, v163
	v_add_f32_e32 v88, v66, v88
	v_add_f32_e32 v89, v74, v89
	v_add_f32_e32 v90, v82, v90
	v_add_f32_e32 v91, v164, v91
	v_add_f32_e32 v88, v67, v88
	v_add_f32_e32 v89, v75, v89
	v_add_f32_e32 v90, v83, v90
	v_add_f32_e32 v91, v165, v91
	v_add_f32_e32 v88, v68, v88
	v_add_f32_e32 v89, v76, v89
	v_add_f32_e32 v90, v84, v90
	v_add_f32_e32 v91, v92, v91
	v_add_f32_e32 v88, v69, v88
	v_add_f32_e32 v89, v77, v89
	v_add_f32_e32 v90, v85, v90
	v_add_f32_e32 v91, v93, v91
	v_add_f32_e32 v88, v70, v88
	v_add_f32_e32 v89, v78, v89
	v_add_f32_e32 v90, v86, v90
	v_add_f32_e32 v91, v94, v91
	v_add_f32_e32 v88, v71, v88
	v_add_f32_e32 v89, v79, v89
	v_add_f32_e32 v90, v87, v90
	v_add_f32_e32 v91, v95, v91
	v_add_f32_e32 v88, v89, v88
	v_add_f32_e32 v89, v91, v90
	v_add_f32_e32 v237, v88, v89
	v_mov_b32_e32 v238, v237
	v_cvt_pk_bf16_f32 v88, v64, v65
	v_cvt_pk_bf16_f32 v89, v66, v67
	v_cvt_pk_bf16_f32 v90, v68, v69
	v_cvt_pk_bf16_f32 v91, v70, v71
	s_nop 1
	v_permlane32_swap_b32_e32 v237, v238
	v_permlane32_swap_b32_e32 v88, v90
	v_permlane32_swap_b32_e32 v89, v91
	v_cvt_pk_bf16_f32 v72, v72, v73
	v_cvt_pk_bf16_f32 v73, v74, v75
	v_cvt_pk_bf16_f32 v74, v76, v77
	v_cvt_pk_bf16_f32 v75, v78, v79
	v_cvt_pk_bf16_f32 v64, v80, v81
	v_cvt_pk_bf16_f32 v65, v82, v83
	v_cvt_pk_bf16_f32 v66, v84, v85
	v_cvt_pk_bf16_f32 v67, v86, v87
	v_cvt_pk_bf16_f32 v68, v162, v163
	v_cvt_pk_bf16_f32 v69, v164, v165
	v_cvt_pk_bf16_f32 v70, v92, v93
	v_cvt_pk_bf16_f32 v71, v94, v95
	v_mfma_f32_32x32x16_bf16 v[96:111], v[166:169], v[170:173], v[96:111]
	v_permlane32_swap_b32_e32 v72, v74
	v_permlane32_swap_b32_e32 v73, v75
	v_permlane32_swap_b32_e32 v64, v66
	v_permlane32_swap_b32_e32 v65, v67
	v_permlane32_swap_b32_e32 v68, v70
	v_permlane32_swap_b32_e32 v69, v71
	v_lshl_add_u64 v[80:81], v[190:191], 0, s[6:7]
	global_load_dwordx4 v[162:165], v[80:81], off
	v_lshl_add_u64 v[80:81], v[192:193], 0, s[6:7]
	v_lshl_add_u64 v[76:77], v[188:189], 0, s[6:7]
	global_load_dwordx4 v[166:169], v[80:81], off
	v_lshl_add_u64 v[80:81], v[198:199], 0, s[6:7]
	global_load_dwordx4 v[76:79], v[76:77], off
	s_nop 0
	global_load_dwordx4 v[174:177], v[80:81], off
	global_load_dwordx4 v[170:173], v[186:187], off
	ds_read_b64_tr_b16 v[80:81], v201 offset:0
	ds_read_b64_tr_b16 v[82:83], v201 offset:0x800
	ds_read_b64_tr_b16 v[84:85], v201 offset:0x1000
	ds_read_b64_tr_b16 v[86:87], v201 offset:0x1800
	ds_read_b64_tr_b16 v[92:93], v201 offset:0x2000
	ds_read_b64_tr_b16 v[94:95], v201 offset:0x2800
	ds_read_b64_tr_b16 v[178:179], v201 offset:0x3000
	ds_read_b64_tr_b16 v[180:181], v201 offset:0x3800
	s_waitcnt lgkmcnt(0)
	s_nop 0
	v_mfma_f32_32x32x16_bf16 v[0:15], v[80:83], v[88:91], v[0:15]
	v_max_f32_e32 v80, v96, v97
	v_max3_f32 v81, v112, v113, v114
	v_max3_f32 v80, v80, v98, v99
	v_max3_f32 v81, v81, v115, v116
	v_max3_f32 v80, v80, v100, v101
	v_mfma_f32_32x32x16_bf16 v[0:15], v[84:87], v[72:75], v[0:15]
	v_max3_f32 v81, v81, v117, v118
	v_max3_f32 v80, v80, v102, v103
	v_max3_f32 v81, v81, v119, v120
	v_max3_f32 v80, v80, v104, v105
	v_max3_f32 v81, v81, v121, v122
	v_max3_f32 v80, v80, v106, v107
	v_max3_f32 v81, v81, v123, v124
	v_mfma_f32_32x32x16_bf16 v[0:15], v[92:95], v[64:67], v[0:15]
	v_max3_f32 v80, v80, v108, v109
	v_max3_f32 v81, v81, v125, v126
	v_max3_f32 v80, v80, v110, v111
	v_max3_f32 v194, v81, v127, v80
	ds_read_b64_tr_b16 v[80:81], v201 offset:0x200
	ds_read_b64_tr_b16 v[82:83], v201 offset:0xa00
	ds_read_b64_tr_b16 v[84:85], v201 offset:0x1200
	v_mfma_f32_32x32x16_bf16 v[0:15], v[178:181], v[68:71], v[0:15]
	ds_read_b64_tr_b16 v[86:87], v201 offset:0x1a00
	ds_read_b64_tr_b16 v[92:93], v201 offset:0x2200
	ds_read_b64_tr_b16 v[94:95], v201 offset:0x2a00
	ds_read_b64_tr_b16 v[178:179], v201 offset:0x3200
	ds_read_b64_tr_b16 v[180:181], v201 offset:0x3a00
	s_waitcnt lgkmcnt(0)
	v_mfma_f32_32x32x16_bf16 v[48:63], v[80:83], v[88:91], v[48:63]
	v_mov_b32_e32 v80, v194
	s_nop 1
	v_permlane32_swap_b32_e32 v194, v80
	v_max_f32_e32 v80, v194, v80
	v_sub_f32_e32 v81, v80, v227
	v_mfma_f32_32x32x16_bf16 v[48:63], v[84:87], v[72:75], v[48:63]
	v_cmp_ge_f32_e32 vcc, s34, v81
	v_max_f32_e32 v80, v227, v80
	v_sub_f32_e32 v81, v227, v80
	v_mul_f32_e32 v81, 0x3dd53b94, v81
	v_exp_f32_e32 v81, v81
	s_cmp_eq_u64 vcc, exec
	v_mfma_f32_32x32x16_bf16 v[48:63], v[92:95], v[64:67], v[48:63]
	s_cselect_b64 vcc, -1, 0
	v_cndmask_b32_e64 v202, v81, 1.0, vcc
	v_cndmask_b32_e32 v227, v80, v227, vcc
	ds_read_b64_tr_b16 v[80:81], v201 offset:0x400
	ds_read_b64_tr_b16 v[82:83], v201 offset:0xc00
	ds_read_b64_tr_b16 v[84:85], v201 offset:0x1400
	ds_read_b64_tr_b16 v[86:87], v201 offset:0x1c00
	v_mfma_f32_32x32x16_bf16 v[48:63], v[178:181], v[68:71], v[48:63]
	ds_read_b64_tr_b16 v[92:93], v201 offset:0x2400
	v_mul_f32_e32 v178, 0xbdd53b94, v227
	ds_read_b64_tr_b16 v[94:95], v201 offset:0x2c00
	v_fmamk_f32 v179, v112, 0x3dd53b94, v178
	v_fmamk_f32 v180, v113, 0x3dd53b94, v178
	ds_read_b64_tr_b16 v[112:113], v201 offset:0x3400
	v_fmamk_f32 v181, v114, 0x3dd53b94, v178
	v_fmamk_f32 v194, v115, 0x3dd53b94, v178
	ds_read_b64_tr_b16 v[114:115], v201 offset:0x3c00
	s_waitcnt lgkmcnt(0)
	v_fmamk_f32 v195, v116, 0x3dd53b94, v178
	v_fmamk_f32 v196, v117, 0x3dd53b94, v178
	v_fmamk_f32 v197, v118, 0x3dd53b94, v178
	v_fmamk_f32 v200, v119, 0x3dd53b94, v178
	v_fmamk_f32 v239, v120, 0x3dd53b94, v178
	v_fmamk_f32 v240, v121, 0x3dd53b94, v178
	v_fmamk_f32 v241, v122, 0x3dd53b94, v178
	v_fmamk_f32 v242, v123, 0x3dd53b94, v178
	v_fmamk_f32 v243, v124, 0x3dd53b94, v178
	v_fmamk_f32 v244, v125, 0x3dd53b94, v178
	v_fmamk_f32 v245, v126, 0x3dd53b94, v178
	v_fmamk_f32 v246, v127, 0x3dd53b94, v178
	v_mfma_f32_32x32x16_bf16 v[32:47], v[80:83], v[88:91], v[32:47]
	v_fma_f32 v116, v100, s54, v178
	v_fma_f32 v117, v101, s54, v178
	v_fma_f32 v118, v102, s54, v178
	v_fma_f32 v119, v103, s54, v178
	v_fma_f32 v120, v104, s54, v178
	v_fma_f32 v121, v105, s54, v178
	v_pk_fma_f32 v[122:123], v[106:107], s[54:55], v[178:179] op_sel_hi:[1,0,0]
	v_exp_f32_e32 v80, v179
	v_exp_f32_e32 v81, v180
	v_exp_f32_e32 v82, v181
	v_mfma_f32_32x32x16_bf16 v[32:47], v[84:87], v[72:75], v[32:47]
	v_exp_f32_e32 v83, v194
	v_exp_f32_e32 v84, v195
	v_exp_f32_e32 v85, v196
	v_exp_f32_e32 v86, v197
	v_exp_f32_e32 v87, v200
	v_pk_fma_f32 v[126:127], v[110:111], s[54:55], v[178:179] op_sel_hi:[1,0,0]
	v_pk_fma_f32 v[124:125], v[108:109], s[54:55], v[178:179] op_sel_hi:[1,0,0]
	v_mfma_f32_32x32x16_bf16 v[32:47], v[92:95], v[64:67], v[32:47]
	ds_read_b64_tr_b16 v[92:93], v201 offset:0x600
	ds_read_b64_tr_b16 v[94:95], v201 offset:0xe00
	v_mfma_f32_32x32x16_bf16 v[32:47], v[112:115], v[68:71], v[32:47]
	v_fma_f32 v112, v96, s54, v178
	v_fma_f32 v113, v97, s54, v178
	ds_read_b64_tr_b16 v[96:97], v201 offset:0x1600
	v_fma_f32 v114, v98, s54, v178
	v_fma_f32 v115, v99, s54, v178
	ds_read_b64_tr_b16 v[98:99], v201 offset:0x1e00
	ds_read_b64_tr_b16 v[100:101], v201 offset:0x2600
	ds_read_b64_tr_b16 v[102:103], v201 offset:0x2e00
	ds_read_b64_tr_b16 v[104:105], v201 offset:0x3600
	ds_read_b64_tr_b16 v[106:107], v201 offset:0x3e00
	s_waitcnt lgkmcnt(0)
	v_mfma_f32_32x32x16_bf16 v[16:31], v[92:95], v[88:91], v[16:31]
	v_exp_f32_e32 v88, v239
	v_exp_f32_e32 v89, v240
	v_exp_f32_e32 v90, v241
	v_exp_f32_e32 v91, v242
	v_exp_f32_e32 v92, v243
	v_exp_f32_e32 v93, v244
	v_exp_f32_e32 v94, v245
	v_mfma_f32_32x32x16_bf16 v[16:31], v[96:99], v[72:75], v[16:31]
	v_exp_f32_e32 v95, v246
	s_barrier
	s_waitcnt vmcnt(0)
	v_cmp_gt_f32_e32 vcc, 1.0, v202
	v_mfma_f32_32x32x16_bf16 v[16:31], v[100:103], v[64:67], v[16:31]
	v_add_u32_e32 v64, 0x10000, v228
	s_waitcnt vmcnt(2)
	ds_write_b128 v205, v[76:79]
	ds_write_b128 v206, v[162:165]
	ds_write_b128 v207, v[166:169] offset:32768
	s_waitcnt vmcnt(1)
	ds_write_b128 v208, v[174:177] offset:32768
	s_waitcnt vmcnt(0)
	ds_write_b128 v64, v[170:173]
	v_mfma_f32_32x32x16_bf16 v[16:31], v[104:107], v[68:71], v[16:31]
	s_cbranch_vccz .LBB0_863
	v_pk_mul_f32 v[14:15], v[14:15], v[202:203] op_sel_hi:[1,0]
	v_pk_mul_f32 v[12:13], v[12:13], v[202:203] op_sel_hi:[1,0]
	v_pk_mul_f32 v[10:11], v[10:11], v[202:203] op_sel_hi:[1,0]
	v_pk_mul_f32 v[8:9], v[8:9], v[202:203] op_sel_hi:[1,0]
	v_pk_mul_f32 v[6:7], v[6:7], v[202:203] op_sel_hi:[1,0]
	v_pk_mul_f32 v[4:5], v[4:5], v[202:203] op_sel_hi:[1,0]
	v_pk_mul_f32 v[2:3], v[2:3], v[202:203] op_sel_hi:[1,0]
	v_pk_mul_f32 v[0:1], v[0:1], v[202:203] op_sel_hi:[1,0]
	v_pk_mul_f32 v[62:63], v[62:63], v[202:203] op_sel_hi:[1,0]
	v_pk_mul_f32 v[60:61], v[60:61], v[202:203] op_sel_hi:[1,0]
	v_pk_mul_f32 v[58:59], v[58:59], v[202:203] op_sel_hi:[1,0]
	v_pk_mul_f32 v[56:57], v[56:57], v[202:203] op_sel_hi:[1,0]
	v_pk_mul_f32 v[54:55], v[54:55], v[202:203] op_sel_hi:[1,0]
	v_pk_mul_f32 v[52:53], v[52:53], v[202:203] op_sel_hi:[1,0]
	v_pk_mul_f32 v[50:51], v[50:51], v[202:203] op_sel_hi:[1,0]
	v_pk_mul_f32 v[48:49], v[48:49], v[202:203] op_sel_hi:[1,0]
	v_pk_mul_f32 v[46:47], v[202:203], v[46:47] op_sel_hi:[0,1]
	v_pk_mul_f32 v[44:45], v[202:203], v[44:45] op_sel_hi:[0,1]
	v_pk_mul_f32 v[42:43], v[202:203], v[42:43] op_sel_hi:[0,1]
	v_pk_mul_f32 v[40:41], v[202:203], v[40:41] op_sel_hi:[0,1]
	v_pk_mul_f32 v[38:39], v[202:203], v[38:39] op_sel_hi:[0,1]
	v_pk_mul_f32 v[36:37], v[202:203], v[36:37] op_sel_hi:[0,1]
	v_pk_mul_f32 v[34:35], v[202:203], v[34:35] op_sel_hi:[0,1]
	v_pk_mul_f32 v[32:33], v[202:203], v[32:33] op_sel_hi:[0,1]
	v_pk_mul_f32 v[30:31], v[202:203], v[30:31] op_sel_hi:[0,1]
	v_pk_mul_f32 v[28:29], v[202:203], v[28:29] op_sel_hi:[0,1]
	v_pk_mul_f32 v[26:27], v[202:203], v[26:27] op_sel_hi:[0,1]
	v_pk_mul_f32 v[24:25], v[202:203], v[24:25] op_sel_hi:[0,1]
	v_pk_mul_f32 v[22:23], v[202:203], v[22:23] op_sel_hi:[0,1]
	v_pk_mul_f32 v[20:21], v[202:203], v[20:21] op_sel_hi:[0,1]
	v_pk_mul_f32 v[18:19], v[202:203], v[18:19] op_sel_hi:[0,1]
	v_pk_mul_f32 v[16:17], v[202:203], v[16:17] op_sel_hi:[0,1]
.LBB0_863:
	s_waitcnt lgkmcnt(0)
	s_barrier
	ds_read_b128 v[64:67], v209 offset:32768
	ds_read_b128 v[68:71], v209 offset:40960
	ds_read_b128 v[162:165], v211 offset:32768
	ds_read_b128 v[166:169], v211 offset:40960
	v_exp_f32_e32 v112, v112
	v_exp_f32_e32 v113, v113
	s_waitcnt lgkmcnt(3)
	v_mfma_f32_32x32x16_bf16 v[96:111], v[64:67], v[158:161], 0
	v_exp_f32_e32 v114, v114
	v_exp_f32_e32 v115, v115
	v_exp_f32_e32 v116, v116
	v_exp_f32_e32 v117, v117
	v_exp_f32_e32 v118, v118
	v_exp_f32_e32 v119, v119
	s_waitcnt lgkmcnt(2)
	v_mfma_f32_32x32x16_bf16 v[64:79], v[68:71], v[158:161], 0
	s_waitcnt lgkmcnt(1)
	v_mfma_f32_32x32x16_bf16 v[96:111], v[162:165], v[154:157], v[96:111]
	s_waitcnt lgkmcnt(0)
	v_mfma_f32_32x32x16_bf16 v[64:79], v[166:169], v[154:157], v[64:79]
	ds_read_b128 v[162:165], v212 offset:32768
	ds_read_b128 v[166:169], v212 offset:40960
	s_waitcnt lgkmcnt(1)
	v_mfma_f32_32x32x16_bf16 v[96:111], v[162:165], v[150:153], v[96:111]
	s_waitcnt lgkmcnt(0)
	v_mfma_f32_32x32x16_bf16 v[64:79], v[166:169], v[150:153], v[64:79]
	ds_read_b128 v[162:165], v213 offset:32768
	ds_read_b128 v[166:169], v213 offset:40960
	s_waitcnt lgkmcnt(1)
	v_mfma_f32_32x32x16_bf16 v[96:111], v[162:165], v[146:149], v[96:111]
	s_waitcnt lgkmcnt(0)
	v_mfma_f32_32x32x16_bf16 v[64:79], v[166:169], v[146:149], v[64:79]
	ds_read_b128 v[162:165], v215 offset:32768
	ds_read_b128 v[166:169], v215 offset:40960
	s_waitcnt lgkmcnt(1)
	v_mfma_f32_32x32x16_bf16 v[96:111], v[162:165], v[142:145], v[96:111]
	s_waitcnt lgkmcnt(0)
	v_mfma_f32_32x32x16_bf16 v[64:79], v[166:169], v[142:145], v[64:79]
	ds_read_b128 v[162:165], v217 offset:32768
	ds_read_b128 v[166:169], v217 offset:40960
	s_waitcnt lgkmcnt(1)
	v_mfma_f32_32x32x16_bf16 v[96:111], v[162:165], v[138:141], v[96:111]
	s_waitcnt lgkmcnt(0)
	v_mfma_f32_32x32x16_bf16 v[64:79], v[166:169], v[138:141], v[64:79]
	ds_read_b128 v[162:165], v214 offset:32768
	ds_read_b128 v[166:169], v214 offset:40960
	s_waitcnt lgkmcnt(1)
	v_mfma_f32_32x32x16_bf16 v[96:111], v[162:165], v[134:137], v[96:111]
	s_waitcnt lgkmcnt(0)
	v_mfma_f32_32x32x16_bf16 v[64:79], v[166:169], v[134:137], v[64:79]
	ds_read_b128 v[162:165], v216 offset:32768
	ds_read_b128 v[166:169], v216 offset:40960
	s_waitcnt lgkmcnt(1)
	v_mfma_f32_32x32x16_bf16 v[96:111], v[162:165], v[130:133], v[96:111]
	s_waitcnt lgkmcnt(0)
	v_mfma_f32_32x32x16_bf16 v[64:79], v[166:169], v[130:133], v[64:79]
	ds_read_b128 v[162:165], v219
	ds_read_b128 v[166:169], v219 offset:4096
	ds_read_b128 v[170:173], v204
	s_waitcnt lgkmcnt(0)
	v_mfma_f32_32x32x16_bf16 v[96:111], v[162:165], v[170:173], v[96:111]
	v_mfma_f32_32x32x16_bf16 v[64:79], v[166:169], v[170:173], v[64:79]
	ds_read_b128 v[162:165], v221
	ds_read_b128 v[166:169], v221 offset:4096
	ds_read_b128 v[170:173], v204 offset:1024
	s_waitcnt lgkmcnt(0)
	v_mfma_f32_32x32x16_bf16 v[96:111], v[162:165], v[170:173], v[96:111]
	v_mfma_f32_32x32x16_bf16 v[64:79], v[166:169], v[170:173], v[64:79]
	ds_read_b128 v[162:165], v223
	ds_read_b128 v[166:169], v223 offset:4096
	ds_read_b128 v[170:173], v204 offset:2048
	s_waitcnt lgkmcnt(0)
	v_mfma_f32_32x32x16_bf16 v[96:111], v[162:165], v[170:173], v[96:111]
	v_mfma_f32_32x32x16_bf16 v[64:79], v[166:169], v[170:173], v[64:79]
	ds_read_b128 v[162:165], v225
	ds_read_b128 v[166:169], v225 offset:4096
	ds_read_b128 v[170:173], v204 offset:3072
	s_waitcnt lgkmcnt(0)
	v_mfma_f32_32x32x16_bf16 v[96:111], v[162:165], v[170:173], v[96:111]
	v_exp_f32_e32 v162, v120
	v_exp_f32_e32 v163, v121
	v_exp_f32_e32 v164, v122
	v_exp_f32_e32 v165, v123
	v_add_f32_e32 v120, v80, v81
	v_add_f32_e32 v121, v88, v89
	v_add_f32_e32 v122, v112, v113
	v_mfma_f32_32x32x16_bf16 v[64:79], v[166:169], v[170:173], v[64:79]
	v_exp_f32_e32 v166, v124
	v_exp_f32_e32 v167, v125
	v_add_f32_e32 v123, v162, v163
	v_exp_f32_e32 v168, v126
	v_add_f32_e32 v120, v82, v120
	v_add_f32_e32 v121, v90, v121
	v_add_f32_e32 v122, v114, v122
	v_add_f32_e32 v123, v164, v123
	v_exp_f32_e32 v169, v127
	v_add_f32_e32 v120, v83, v120
	v_add_f32_e32 v121, v91, v121
	v_add_f32_e32 v122, v115, v122
	v_add_f32_e32 v123, v165, v123
	v_add_f32_e32 v120, v84, v120
	v_add_f32_e32 v121, v92, v121
	v_add_f32_e32 v122, v116, v122
	v_add_f32_e32 v123, v166, v123
	v_add_f32_e32 v120, v85, v120
	v_add_f32_e32 v121, v93, v121
	v_add_f32_e32 v122, v117, v122
	v_add_f32_e32 v123, v167, v123
	v_add_f32_e32 v120, v86, v120
	v_add_f32_e32 v121, v94, v121
	v_add_f32_e32 v122, v118, v122
	v_add_f32_e32 v123, v168, v123
	v_add_f32_e32 v120, v87, v120
	v_add_f32_e32 v121, v95, v121
	v_add_f32_e32 v122, v119, v122
	v_add_f32_e32 v123, v169, v123
	v_add_f32_e32 v120, v121, v120
	v_add_f32_e32 v121, v123, v122
	v_add_f32_e32 v239, v120, v121
	v_mov_b32_e32 v240, v239
	s_nop 1
	v_permlane32_swap_b32_e32 v239, v240
	v_cvt_pk_bf16_f32 v124, v80, v81
	v_cvt_pk_bf16_f32 v125, v82, v83
	v_cvt_pk_bf16_f32 v126, v84, v85
	v_cvt_pk_bf16_f32 v127, v86, v87
	v_cvt_pk_bf16_f32 v120, v88, v89
	v_cvt_pk_bf16_f32 v121, v90, v91
	v_cvt_pk_bf16_f32 v122, v92, v93
	v_cvt_pk_bf16_f32 v123, v94, v95
	v_cvt_pk_bf16_f32 v112, v112, v113
	v_cvt_pk_bf16_f32 v113, v114, v115
	v_cvt_pk_bf16_f32 v114, v116, v117
	v_cvt_pk_bf16_f32 v115, v118, v119
	v_cvt_pk_bf16_f32 v116, v162, v163
	v_cvt_pk_bf16_f32 v117, v164, v165
	v_cvt_pk_bf16_f32 v118, v166, v167
	v_cvt_pk_bf16_f32 v119, v168, v169
	s_nop 0
	v_permlane32_swap_b32_e32 v124, v126
	v_permlane32_swap_b32_e32 v125, v127
	v_permlane32_swap_b32_e32 v120, v122
	v_permlane32_swap_b32_e32 v121, v123
	v_permlane32_swap_b32_e32 v112, v114
	v_permlane32_swap_b32_e32 v113, v115
	v_permlane32_swap_b32_e32 v116, v118
	v_permlane32_swap_b32_e32 v117, v119
	s_add_i32 s2, s20, 1
	s_min_i32 s2, s2, s23
	s_lshl_b32 s72, s2, 6
	s_mul_i32 s2, s72, s62
	s_mov_b32 s3, s73
	s_lshl_b64 s[2:3], s[2:3], 1
	s_add_u32 s24, s18, s2
	s_addc_u32 s25, s19, s3
	s_add_u32 s2, s16, s2
	s_addc_u32 s3, s17, s3
	global_load_dwordx4 v[162:165], v128, s[24:25]
	global_load_dwordx4 v[166:169], v182, s[24:25]
	global_load_dwordx4 v[170:173], v128, s[2:3]
	global_load_dwordx4 v[174:177], v182, s[2:3]
	s_lshl_b64 s[2:3], s[72:73], 7
	v_lshl_add_u64 v[80:81], v[184:185], 0, s[2:3]
	global_load_dwordx4 v[178:181], v[80:81], off
	ds_read_b64_tr_b16 v[80:81], v203 offset:0
	ds_read_b64_tr_b16 v[82:83], v203 offset:0x800
	ds_read_b64_tr_b16 v[84:85], v203 offset:0x1000
	ds_read_b64_tr_b16 v[86:87], v203 offset:0x1800
	ds_read_b64_tr_b16 v[88:89], v203 offset:0x2000
	ds_read_b64_tr_b16 v[90:91], v203 offset:0x2800
	ds_read_b64_tr_b16 v[92:93], v203 offset:0x3000
	ds_read_b64_tr_b16 v[94:95], v203 offset:0x3800
	s_waitcnt lgkmcnt(0)
	s_nop 0
	v_mfma_f32_32x32x16_bf16 v[0:15], v[80:83], v[124:127], v[0:15]
	v_max_f32_e32 v80, v64, v65
	v_max3_f32 v81, v96, v97, v98
	v_max3_f32 v80, v80, v66, v67
	v_max3_f32 v81, v81, v99, v100
	v_max3_f32 v80, v80, v68, v69
	v_mfma_f32_32x32x16_bf16 v[0:15], v[84:87], v[120:123], v[0:15]
	v_max3_f32 v81, v81, v101, v102
	v_max3_f32 v80, v80, v70, v71
	v_max3_f32 v81, v81, v103, v104
	v_max3_f32 v80, v80, v72, v73
	v_max3_f32 v81, v81, v105, v106
	v_max3_f32 v80, v80, v74, v75
	v_max3_f32 v81, v81, v107, v108
	v_mfma_f32_32x32x16_bf16 v[0:15], v[88:91], v[112:115], v[0:15]
	v_max3_f32 v80, v80, v76, v77
	v_max3_f32 v81, v81, v109, v110
	v_max3_f32 v80, v80, v78, v79
	v_max3_f32 v194, v81, v111, v80
	ds_read_b64_tr_b16 v[80:81], v203 offset:0x200
	ds_read_b64_tr_b16 v[82:83], v203 offset:0xa00
	ds_read_b64_tr_b16 v[84:85], v203 offset:0x1200
	v_mfma_f32_32x32x16_bf16 v[0:15], v[92:95], v[116:119], v[0:15]
	ds_read_b64_tr_b16 v[86:87], v203 offset:0x1a00
	ds_read_b64_tr_b16 v[88:89], v203 offset:0x2200
	ds_read_b64_tr_b16 v[90:91], v203 offset:0x2a00
	ds_read_b64_tr_b16 v[92:93], v203 offset:0x3200
	ds_read_b64_tr_b16 v[94:95], v203 offset:0x3a00
	s_waitcnt lgkmcnt(0)
	v_mfma_f32_32x32x16_bf16 v[48:63], v[80:83], v[124:127], v[48:63]
	v_mov_b32_e32 v80, v194
	s_nop 1
	v_permlane32_swap_b32_e32 v194, v80
	v_max_f32_e32 v80, v194, v80
	v_sub_f32_e32 v81, v80, v227
	v_mfma_f32_32x32x16_bf16 v[48:63], v[84:87], v[120:123], v[48:63]
	v_cmp_ge_f32_e32 vcc, s34, v81
	v_max_f32_e32 v80, v227, v80
	v_sub_f32_e32 v81, v227, v80
	v_mul_f32_e32 v81, 0x3dd53b94, v81
	v_exp_f32_e32 v81, v81
	s_cmp_eq_u64 vcc, exec
	v_mfma_f32_32x32x16_bf16 v[48:63], v[88:91], v[112:115], v[48:63]
	s_cselect_b64 vcc, -1, 0
	v_cndmask_b32_e64 v200, v81, 1.0, vcc
	v_cndmask_b32_e32 v227, v80, v227, vcc
	ds_read_b64_tr_b16 v[80:81], v203 offset:0x400
	ds_read_b64_tr_b16 v[82:83], v203 offset:0xc00
	ds_read_b64_tr_b16 v[84:85], v203 offset:0x1400
	ds_read_b64_tr_b16 v[86:87], v203 offset:0x1c00
	v_mfma_f32_32x32x16_bf16 v[48:63], v[92:95], v[116:119], v[48:63]
	ds_read_b64_tr_b16 v[88:89], v203 offset:0x2400
	ds_read_b64_tr_b16 v[90:91], v203 offset:0x2c00
	ds_read_b64_tr_b16 v[92:93], v203 offset:0x3400
	ds_read_b64_tr_b16 v[94:95], v203 offset:0x3c00
	s_waitcnt lgkmcnt(0)
	v_mul_f32_e32 v242, 0xbdd53b94, v227
	v_fmamk_f32 v96, v96, 0x3dd53b94, v242
	v_fmamk_f32 v97, v97, 0x3dd53b94, v242
	v_fmamk_f32 v98, v98, 0x3dd53b94, v242
	v_fmamk_f32 v99, v99, 0x3dd53b94, v242
	v_fmamk_f32 v100, v100, 0x3dd53b94, v242
	v_fmamk_f32 v101, v101, 0x3dd53b94, v242
	v_fmamk_f32 v102, v102, 0x3dd53b94, v242
	v_fmamk_f32 v103, v103, 0x3dd53b94, v242
	v_fmamk_f32 v194, v104, 0x3dd53b94, v242
	v_fmamk_f32 v195, v105, 0x3dd53b94, v242
	v_fmamk_f32 v196, v106, 0x3dd53b94, v242
	v_fmamk_f32 v197, v107, 0x3dd53b94, v242
	v_fmamk_f32 v108, v108, 0x3dd53b94, v242
	v_fmamk_f32 v109, v109, 0x3dd53b94, v242
	v_fmamk_f32 v110, v110, 0x3dd53b94, v242
	v_fmamk_f32 v111, v111, 0x3dd53b94, v242
	v_mfma_f32_32x32x16_bf16 v[32:47], v[80:83], v[124:127], v[32:47]
	v_fma_f32 v80, v64, s54, v242
	v_fma_f32 v81, v65, s54, v242
	v_exp_f32_e32 v64, v96
	v_exp_f32_e32 v65, v97
	v_pk_fma_f32 v[82:83], v[66:67], s[54:55], v[242:243] op_sel_hi:[1,0,0]
	v_exp_f32_e32 v66, v98
	v_exp_f32_e32 v67, v99
	v_mfma_f32_32x32x16_bf16 v[32:47], v[84:87], v[120:123], v[32:47]
	v_fma_f32 v84, v68, s54, v242
	v_fma_f32 v85, v69, s54, v242
	v_exp_f32_e32 v68, v100
	v_exp_f32_e32 v69, v101
	v_pk_fma_f32 v[86:87], v[70:71], s[54:55], v[242:243] op_sel_hi:[1,0,0]
	v_exp_f32_e32 v70, v102
	v_exp_f32_e32 v71, v103
	v_mfma_f32_32x32x16_bf16 v[32:47], v[88:91], v[112:115], v[32:47]
	v_fma_f32 v88, v72, s54, v242
	v_fma_f32 v89, v73, s54, v242
	ds_read_b64_tr_b16 v[72:73], v203 offset:0x600
	v_fma_f32 v90, v74, s54, v242
	v_fma_f32 v91, v75, s54, v242
	ds_read_b64_tr_b16 v[74:75], v203 offset:0xe00
	ds_read_b64_tr_b16 v[96:97], v203 offset:0x1600
	ds_read_b64_tr_b16 v[98:99], v203 offset:0x1e00
	ds_read_b64_tr_b16 v[100:101], v203 offset:0x2600
	v_mfma_f32_32x32x16_bf16 v[32:47], v[92:95], v[116:119], v[32:47]
	ds_read_b64_tr_b16 v[102:103], v203 offset:0x2e00
	ds_read_b64_tr_b16 v[104:105], v203 offset:0x3600
	ds_read_b64_tr_b16 v[106:107], v203 offset:0x3e00
	s_waitcnt lgkmcnt(0)
	v_fma_f32 v94, v78, s54, v242
	v_fma_f32 v95, v79, s54, v242
	v_fma_f32 v92, v76, s54, v242
	v_fma_f32 v93, v77, s54, v242
	v_mfma_f32_32x32x16_bf16 v[16:31], v[72:75], v[124:127], v[16:31]
	v_exp_f32_e32 v72, v194
	v_exp_f32_e32 v73, v195
	v_exp_f32_e32 v74, v196
	v_exp_f32_e32 v75, v197
	v_exp_f32_e32 v76, v108
	v_exp_f32_e32 v77, v109
	v_exp_f32_e32 v78, v110
	v_mfma_f32_32x32x16_bf16 v[16:31], v[96:99], v[120:123], v[16:31]
	v_exp_f32_e32 v79, v111
	s_barrier
	s_waitcnt vmcnt(0)
	v_cmp_gt_f32_e32 vcc, 1.0, v200
	v_mfma_f32_32x32x16_bf16 v[16:31], v[100:103], v[112:115], v[16:31]
	s_waitcnt vmcnt(4)
	ds_write_b128 v205, v[162:165] offset:16384
	s_waitcnt vmcnt(3)
	ds_write_b128 v206, v[166:169] offset:16384
	s_waitcnt vmcnt(2)
	ds_write_b128 v207, v[170:173] offset:49152
	s_waitcnt vmcnt(1)
	ds_write_b128 v208, v[174:177] offset:49152
	s_waitcnt vmcnt(0)
	ds_write_b128 v229, v[178:181]
	v_mfma_f32_32x32x16_bf16 v[16:31], v[104:107], v[116:119], v[16:31]
	s_cbranch_vccz .LBB0_865
	v_pk_mul_f32 v[14:15], v[14:15], v[200:201] op_sel_hi:[1,0]
	v_pk_mul_f32 v[12:13], v[12:13], v[200:201] op_sel_hi:[1,0]
	v_pk_mul_f32 v[10:11], v[10:11], v[200:201] op_sel_hi:[1,0]
	v_pk_mul_f32 v[8:9], v[8:9], v[200:201] op_sel_hi:[1,0]
	v_pk_mul_f32 v[6:7], v[6:7], v[200:201] op_sel_hi:[1,0]
	v_pk_mul_f32 v[4:5], v[4:5], v[200:201] op_sel_hi:[1,0]
	v_pk_mul_f32 v[2:3], v[2:3], v[200:201] op_sel_hi:[1,0]
	v_pk_mul_f32 v[0:1], v[0:1], v[200:201] op_sel_hi:[1,0]
	v_pk_mul_f32 v[62:63], v[62:63], v[200:201] op_sel_hi:[1,0]
	v_pk_mul_f32 v[60:61], v[60:61], v[200:201] op_sel_hi:[1,0]
	v_pk_mul_f32 v[58:59], v[58:59], v[200:201] op_sel_hi:[1,0]
	v_pk_mul_f32 v[56:57], v[56:57], v[200:201] op_sel_hi:[1,0]
	v_pk_mul_f32 v[54:55], v[54:55], v[200:201] op_sel_hi:[1,0]
	v_pk_mul_f32 v[52:53], v[52:53], v[200:201] op_sel_hi:[1,0]
	v_pk_mul_f32 v[50:51], v[50:51], v[200:201] op_sel_hi:[1,0]
	v_pk_mul_f32 v[48:49], v[48:49], v[200:201] op_sel_hi:[1,0]
	v_pk_mul_f32 v[46:47], v[200:201], v[46:47] op_sel_hi:[0,1]
	v_pk_mul_f32 v[44:45], v[200:201], v[44:45] op_sel_hi:[0,1]
	v_pk_mul_f32 v[42:43], v[200:201], v[42:43] op_sel_hi:[0,1]
	v_pk_mul_f32 v[40:41], v[200:201], v[40:41] op_sel_hi:[0,1]
	v_pk_mul_f32 v[38:39], v[200:201], v[38:39] op_sel_hi:[0,1]
	v_pk_mul_f32 v[36:37], v[200:201], v[36:37] op_sel_hi:[0,1]
	v_pk_mul_f32 v[34:35], v[200:201], v[34:35] op_sel_hi:[0,1]
	v_pk_mul_f32 v[32:33], v[200:201], v[32:33] op_sel_hi:[0,1]
	v_pk_mul_f32 v[30:31], v[200:201], v[30:31] op_sel_hi:[0,1]
	v_pk_mul_f32 v[28:29], v[200:201], v[28:29] op_sel_hi:[0,1]
	v_pk_mul_f32 v[26:27], v[200:201], v[26:27] op_sel_hi:[0,1]
	v_pk_mul_f32 v[24:25], v[200:201], v[24:25] op_sel_hi:[0,1]
	v_pk_mul_f32 v[22:23], v[200:201], v[22:23] op_sel_hi:[0,1]
	v_pk_mul_f32 v[20:21], v[200:201], v[20:21] op_sel_hi:[0,1]
	v_pk_mul_f32 v[18:19], v[200:201], v[18:19] op_sel_hi:[0,1]
	v_pk_mul_f32 v[16:17], v[200:201], v[16:17] op_sel_hi:[0,1]
